# v33: SGU unit prologue de-serialised: 8 X-row loads + rstd load + 8 weight-row loads issued together with counted waits (was 17 load/vmcnt(0) round trips per unit)
# speedup vs baseline: 1.0021x; 1.0021x over previous
; #define GAS __attribute__((address_space(1)))
; #define LAS __attribute__((address_space(3)))
; __device__ __forceinline__ unsigned pk2(float lo, float hi) { return pg8::cvt_pk_bf16(lo, hi); }
; __device__ __forceinline__ void sgu_unit(Frame& F, int unit) {
;     ...
;     __syncthreads();
; #pragma unroll
;     for (int i = 0; i < 8; ++i) *(LAS v4u*)(L + (rs_ + 16 * i) * 512 + q_ * 16) = *(const GAS v4u*)(F.PROJ + (size_t)(r0 + rs_ + 16 * i) * PNP + PGV + c0 + 8 * q_);
;     { const f32x4 q = *(const GAS f32x4*)(F.RS + r0 + 4 * q_);
; #pragma unroll
;       for (int i = 0; i < 8; ++i) { const int t_ = rs_ + 16 * i; const f32x4 wv = *(const GAS f32x4*)(F.sgw + ((size_t)(g * GMC + t_)) * GMC + 4 * q_);
;           const int sb = 4 * q_; v2u o;
;           o.x = pk2(sb + 0 <= t_ ? wv.x * q.x : 0.f, sb + 1 <= t_ ? wv.y * q.y : 0.f); o.y = pk2(sb + 2 <= t_ ? wv.z * q.z : 0.f, sb + 3 <= t_ ? wv.w * q.w : 0.f);
;           *(LAS v2u*)(L + SG_WOFF + t_ * SG_STR + 8 * q_) = o; } }
;     __syncthreads();
;     v4u uu[8];
; #pragma unroll
;     for (int i = 0; i < 8; ++i) uu[i] = *(const GAS v4u*)(F.PROJ + (size_t)(r0 + rs_ + 16 * i) * PNP + PGU + c0 + 8 * q_);
.LBB0_1330:
	s_and_b32 s74, s33, 0xffffff80
	s_and_b32 s83, s82, 7
	v_or_b32_e32 v128, s74, v1
	v_mad_i64_i32 v[2:3], s[0:1], v128, s77, v[108:109]
	s_lshl_b32 s84, s83, 9
	s_mov_b32 s85, s73
	v_lshl_add_u64 v[2:3], v[2:3], 0, s[84:85]
	v_lshl_add_u64 v[2:3], v[2:3], 0, v[110:111]
	v_add_co_u32_e64 v4, s[0:1], s78, v2
	s_nop 1
	v_addc_co_u32_e64 v5, s[0:1], 0, v3, s[0:1]
	s_barrier
	global_load_dwordx4 v[28:31], v[4:5], off offset:2048
	v_or_b32_e32 v126, 16, v128
	v_or_b32_e32 v124, 32, v128
	v_or_b32_e32 v122, 48, v128
	v_or_b32_e32 v120, 64, v128
	v_or_b32_e32 v118, 0x50, v128
	v_or_b32_e32 v116, 0x60, v128
	v_or_b32_e32 v114, 0x70, v128
	s_ashr_i32 s75, s74, 31
	v_ashrrev_i32_e32 v129, 31, v128
	s_lshl_b32 s72, s83, 8
	v_ashrrev_i32_e32 v127, 31, v126
	v_ashrrev_i32_e32 v125, 31, v124
	v_ashrrev_i32_e32 v123, 31, v122
	v_ashrrev_i32_e32 v121, 31, v120
	v_ashrrev_i32_e32 v119, 31, v118
	v_ashrrev_i32_e32 v117, 31, v116
	v_ashrrev_i32_e32 v115, 31, v114
	v_readlane_b32 s89, v248, 15
	s_add_i32 s82, s82, s89
	s_add_i32 s33, s33, s76
	v_mad_i64_i32 v[4:5], s[0:1], v126, s77, v[108:109]
	v_lshl_add_u64 v[4:5], v[4:5], 0, s[84:85]
	v_lshl_add_u64 v[4:5], v[4:5], 0, v[110:111]
	v_add_co_u32_e64 v26, s[0:1], s78, v4
	s_nop 1
	v_addc_co_u32_e64 v27, s[0:1], 0, v5, s[0:1]
	global_load_dwordx4 v[32:35], v[26:27], off offset:2048
	v_mad_i64_i32 v[6:7], s[0:1], v124, s77, v[108:109]
	v_lshl_add_u64 v[6:7], v[6:7], 0, s[84:85]
	v_lshl_add_u64 v[6:7], v[6:7], 0, v[110:111]
	v_add_co_u32_e64 v26, s[0:1], s78, v6
	s_nop 1
	v_addc_co_u32_e64 v27, s[0:1], 0, v7, s[0:1]
	global_load_dwordx4 v[36:39], v[26:27], off offset:2048
	v_mad_i64_i32 v[8:9], s[0:1], v122, s77, v[108:109]
	v_lshl_add_u64 v[8:9], v[8:9], 0, s[84:85]
	v_lshl_add_u64 v[8:9], v[8:9], 0, v[110:111]
	v_add_co_u32_e64 v26, s[0:1], s78, v8
	s_nop 1
	v_addc_co_u32_e64 v27, s[0:1], 0, v9, s[0:1]
	global_load_dwordx4 v[40:43], v[26:27], off offset:2048
	v_mad_i64_i32 v[10:11], s[0:1], v120, s77, v[108:109]
	v_lshl_add_u64 v[10:11], v[10:11], 0, s[84:85]
	v_lshl_add_u64 v[10:11], v[10:11], 0, v[110:111]
	v_add_co_u32_e64 v26, s[0:1], s78, v10
	s_nop 1
	v_addc_co_u32_e64 v27, s[0:1], 0, v11, s[0:1]
	global_load_dwordx4 v[44:47], v[26:27], off offset:2048
	v_mad_i64_i32 v[12:13], s[0:1], v118, s77, v[108:109]
	v_lshl_add_u64 v[12:13], v[12:13], 0, s[84:85]
	v_lshl_add_u64 v[12:13], v[12:13], 0, v[110:111]
	v_add_co_u32_e64 v26, s[0:1], s78, v12
	s_nop 1
	v_addc_co_u32_e64 v27, s[0:1], 0, v13, s[0:1]
	global_load_dwordx4 v[48:51], v[26:27], off offset:2048
	v_mad_i64_i32 v[14:15], s[0:1], v116, s77, v[108:109]
	v_lshl_add_u64 v[14:15], v[14:15], 0, s[84:85]
	v_lshl_add_u64 v[14:15], v[14:15], 0, v[110:111]
	v_add_co_u32_e64 v26, s[0:1], s78, v14
	s_nop 1
	v_addc_co_u32_e64 v27, s[0:1], 0, v15, s[0:1]
	global_load_dwordx4 v[52:55], v[26:27], off offset:2048
	v_mad_i64_i32 v[16:17], s[0:1], v114, s77, v[108:109]
	v_lshl_add_u64 v[16:17], v[16:17], 0, s[84:85]
	v_lshl_add_u64 v[16:17], v[16:17], 0, v[110:111]
	v_add_co_u32_e64 v26, s[0:1], s78, v16
	s_nop 1
	v_addc_co_u32_e64 v27, s[0:1], 0, v17, s[0:1]
	global_load_dwordx4 v[56:59], v[26:27], off offset:2048
	s_lshl_b32 s0, s83, 7
	v_or_b32_e32 v113, s0, v1
	v_lshl_add_u64 v[18:19], s[74:75], 2, v[102:103]
	global_load_dwordx4 v[18:21], v[18:19], off
	v_lshlrev_b32_e32 v100, 9, v113
	v_lshl_add_u64 v[22:23], v[104:105], 0, v[100:101]
	global_load_dwordx4 v[60:63], v[22:23], off
	v_or_b32_e32 v22, s0, v130
	v_lshlrev_b32_e32 v100, 9, v22
	v_lshl_add_u64 v[22:23], v[104:105], 0, v[100:101]
	global_load_dwordx4 v[64:67], v[22:23], off
	v_or_b32_e32 v22, s0, v131
	v_lshlrev_b32_e32 v100, 9, v22
	v_lshl_add_u64 v[22:23], v[104:105], 0, v[100:101]
	global_load_dwordx4 v[68:71], v[22:23], off
	v_or_b32_e32 v22, s0, v132
	v_lshlrev_b32_e32 v100, 9, v22
	v_lshl_add_u64 v[22:23], v[104:105], 0, v[100:101]
	global_load_dwordx4 v[72:75], v[22:23], off
	v_or_b32_e32 v22, s0, v133
	v_lshlrev_b32_e32 v100, 9, v22
	v_lshl_add_u64 v[22:23], v[104:105], 0, v[100:101]
	global_load_dwordx4 v[76:79], v[22:23], off
	v_or_b32_e32 v22, s0, v134
	v_lshlrev_b32_e32 v100, 9, v22
	v_lshl_add_u64 v[22:23], v[104:105], 0, v[100:101]
	global_load_dwordx4 v[80:83], v[22:23], off
	v_or_b32_e32 v22, s0, v135
	v_lshlrev_b32_e32 v100, 9, v22
	v_lshl_add_u64 v[22:23], v[104:105], 0, v[100:101]
	global_load_dwordx4 v[84:87], v[22:23], off
	v_or_b32_e32 v22, s0, v136
	v_lshlrev_b32_e32 v100, 9, v22
	v_lshl_add_u64 v[22:23], v[104:105], 0, v[100:101]
	global_load_dwordx4 v[88:91], v[22:23], off
	s_waitcnt vmcnt(16)
	ds_write_b128 v139, v[28:31]
	s_waitcnt vmcnt(15)
	ds_write_b128 v140, v[32:35]
	s_waitcnt vmcnt(14)
	ds_write_b128 v141, v[36:39]
	s_waitcnt vmcnt(13)
	ds_write_b128 v142, v[40:43]
	s_waitcnt vmcnt(12)
	ds_write_b128 v143, v[44:47]
	s_waitcnt vmcnt(11)
	ds_write_b128 v144, v[48:51]
	s_waitcnt vmcnt(10)
	ds_write_b128 v145, v[52:55]
	s_waitcnt vmcnt(9)
	ds_write_b128 v146, v[56:59]
	s_waitcnt vmcnt(7)
	v_mul_f32_e32 v22, v18, v60
	v_mul_f32_e32 v23, v19, v61
	v_cndmask_b32_e64 v22, v22, 0, s[70:71]
	v_cndmask_b32_e64 v23, 0, v23, s[4:5]
	v_cvt_pk_bf16_f32 v22, v22, v23
	v_mul_f32_e32 v23, v20, v62
	v_cndmask_b32_e64 v23, v23, 0, s[6:7]
	v_mul_f32_e32 v24, v21, v63
	v_cndmask_b32_e64 v24, v24, 0, s[86:87]
	v_cvt_pk_bf16_f32 v23, v23, v24
	ds_write_b64 v147, v[22:23]
	s_waitcnt vmcnt(6)
	v_mul_f32_e32 v22, v18, v64
	v_mul_f32_e32 v23, v19, v65
	v_cndmask_b32_e64 v22, v22, 0, s[90:91]
	v_cndmask_b32_e64 v23, 0, v23, s[92:93]
	v_cvt_pk_bf16_f32 v22, v22, v23
	v_mul_f32_e32 v23, v20, v66
	v_cndmask_b32_e64 v23, v23, 0, s[94:95]
	v_mul_f32_e32 v24, v21, v67
	v_cndmask_b32_e64 v24, v24, 0, s[96:97]
	v_cvt_pk_bf16_f32 v23, v23, v24
	ds_write_b64 v147, v[22:23] offset:4352
	s_waitcnt vmcnt(5)
; #define GAS __attribute__((address_space(1)))
; #define LAS __attribute__((address_space(3)))
; __device__ __forceinline__ unsigned pk2(float lo, float hi) { return pg8::cvt_pk_bf16(lo, hi); }
; __device__ __forceinline__ void sgu_unit(Frame& F, int unit) {
;     ...
;       for (int i = 0; i < 8; ++i) { const int t_ = rs_ + 16 * i; const f32x4 wv = *(const GAS f32x4*)(F.sgw + ((size_t)(g * GMC + t_)) * GMC + 4 * q_);
;           const int sb = 4 * q_; v2u o;
;           o.x = pk2(sb + 0 <= t_ ? wv.x * q.x : 0.f, sb + 1 <= t_ ? wv.y * q.y : 0.f); o.y = pk2(sb + 2 <= t_ ? wv.z * q.z : 0.f, sb + 3 <= t_ ? wv.w * q.w : 0.f);
;           *(LAS v2u*)(L + SG_WOFF + t_ * SG_STR + 8 * q_) = o; } }
;     __syncthreads();
;     v4u uu[8];
; #pragma unroll
;     for (int i = 0; i < 8; ++i) uu[i] = *(const GAS v4u*)(F.PROJ + (size_t)(r0 + rs_ + 16 * i) * PNP + PGU + c0 + 8 * q_);
;     f32x16 acc[4];
; #pragma unroll
;     for (int tb = 0; tb < 4; ++tb)
; #pragma unroll
;         for (int r = 0; r < 16; ++r) acc[tb][r] = 0.f;
;     const LAS unsigned char* xb = L + hi * 8 * 512 + 2 * (32 * w + l31);
;     const LAS unsigned char* wa = L + SG_WOFF + l31 * SG_STR + hi * 16;
; #pragma unroll
;     for (int ks = 0; ks < 8; ++ks) {
;         v4u xw;
; #pragma unroll
;         for (int j = 0; j < 4; ++j) { const unsigned lo = *(const LAS unsigned short*)(xb + (16 * ks + 2 * j) * 512), hh = *(const LAS unsigned short*)(xb + (16 * ks + 2 * j + 1) * 512); xw[j] = lo | (hh << 16); }
;         const bf16x8 xf = __builtin_bit_cast(bf16x8, xw);
; #pragma unroll
;         for (int tb = 0; tb < 4; ++tb) if (ks < 2 * (tb + 1)) { const bf16x8 wf = *(const LAS bf16x8*)(wa + tb * 32 * SG_STR + ks * 32); acc[tb] = __builtin_amdgcn_mfma_f32_32x32x16_bf16(wf, xf, acc[tb], 0, 0, 0); } }
	v_mul_f32_e32 v22, v18, v68
	v_mul_f32_e32 v23, v19, v69
	v_cndmask_b32_e64 v22, v22, 0, vcc
	v_cndmask_b32_e64 v23, 0, v23, s[2:3]
	v_cvt_pk_bf16_f32 v22, v22, v23
	v_mul_f32_e32 v23, v20, v70
	v_cndmask_b32_e64 v23, v23, 0, s[20:21]
	v_mul_f32_e32 v24, v21, v71
	v_cndmask_b32_e64 v24, v24, 0, s[22:23]
	v_cvt_pk_bf16_f32 v23, v23, v24
	ds_write_b64 v147, v[22:23] offset:8704
	s_waitcnt vmcnt(4)
	v_mul_f32_e32 v22, v18, v72
	v_mul_f32_e32 v23, v19, v73
	v_cndmask_b32_e64 v22, v22, 0, s[24:25]
	v_cndmask_b32_e64 v23, 0, v23, s[26:27]
	v_cvt_pk_bf16_f32 v22, v22, v23
	v_mul_f32_e32 v23, v20, v74
	v_cndmask_b32_e64 v23, v23, 0, s[28:29]
	v_mul_f32_e32 v24, v21, v75
	v_cndmask_b32_e64 v24, v24, 0, s[30:31]
	v_cvt_pk_bf16_f32 v23, v23, v24
	ds_write_b64 v147, v[22:23] offset:13056
	s_waitcnt vmcnt(3)
	v_mul_f32_e32 v22, v18, v76
	v_mul_f32_e32 v23, v19, v77
	v_cndmask_b32_e64 v22, v22, 0, s[34:35]
	v_cndmask_b32_e64 v23, 0, v23, s[36:37]
	v_cvt_pk_bf16_f32 v22, v22, v23
	v_mul_f32_e32 v23, v20, v78
	v_cndmask_b32_e64 v23, v23, 0, s[38:39]
	v_mul_f32_e32 v24, v21, v79
	v_cndmask_b32_e64 v24, v24, 0, s[40:41]
	v_cvt_pk_bf16_f32 v23, v23, v24
	ds_write_b64 v147, v[22:23] offset:17408
	s_waitcnt vmcnt(2)
	v_mul_f32_e32 v22, v18, v80
	v_mul_f32_e32 v23, v19, v81
	v_cndmask_b32_e64 v22, v22, 0, s[42:43]
	v_cndmask_b32_e64 v23, 0, v23, s[66:67]
	v_cvt_pk_bf16_f32 v22, v22, v23
	v_mul_f32_e32 v23, v20, v82
	v_cndmask_b32_e64 v23, v23, 0, s[46:47]
	v_mul_f32_e32 v24, v21, v83
	v_cndmask_b32_e64 v24, v24, 0, s[48:49]
	v_cvt_pk_bf16_f32 v23, v23, v24
	ds_write_b64 v147, v[22:23] offset:21760
	s_waitcnt vmcnt(1)
	v_mul_f32_e32 v22, v18, v84
	v_mul_f32_e32 v23, v19, v85
	v_cndmask_b32_e64 v22, v22, 0, s[50:51]
	v_cndmask_b32_e64 v23, 0, v23, s[52:53]
	v_cvt_pk_bf16_f32 v22, v22, v23
	v_mul_f32_e32 v23, v20, v86
	v_cndmask_b32_e64 v23, v23, 0, s[54:55]
	v_mul_f32_e32 v24, v21, v87
	v_cndmask_b32_e64 v24, v24, 0, s[56:57]
	v_cvt_pk_bf16_f32 v23, v23, v24
	ds_write_b64 v147, v[22:23] offset:26112
	s_waitcnt vmcnt(0)
	v_add_co_u32_e64 v2, s[0:1], s79, v2
	v_mul_f32_e32 v18, v18, v88
	v_mul_f32_e32 v19, v19, v89
	v_cndmask_b32_e64 v18, v18, 0, s[58:59]
	v_cndmask_b32_e64 v19, 0, v19, s[60:61]
	v_cvt_pk_bf16_f32 v18, v18, v19
	v_mul_f32_e32 v19, v20, v90
	v_cndmask_b32_e64 v19, v19, 0, s[62:63]
	v_mul_f32_e32 v20, v21, v91
	v_addc_co_u32_e64 v3, s[0:1], 0, v3, s[0:1]
	v_cndmask_b32_e64 v20, v20, 0, s[64:65]
	v_cvt_pk_bf16_f32 v19, v19, v20
	ds_write_b64 v147, v[18:19] offset:30464
	s_waitcnt lgkmcnt(0)
	s_barrier
	global_load_dwordx4 v[94:97], v[2:3], off offset:2048
	v_add_co_u32_e64 v2, s[0:1], s79, v4
	s_nop 1
	v_addc_co_u32_e64 v3, s[0:1], 0, v5, s[0:1]
	global_load_dwordx4 v[90:93], v[2:3], off offset:2048
	v_add_co_u32_e64 v2, s[0:1], s79, v6
	s_nop 1
	v_addc_co_u32_e64 v3, s[0:1], 0, v7, s[0:1]
	global_load_dwordx4 v[86:89], v[2:3], off offset:2048
	v_add_co_u32_e64 v2, s[0:1], s79, v8
	s_nop 1
	v_addc_co_u32_e64 v3, s[0:1], 0, v9, s[0:1]
	global_load_dwordx4 v[82:85], v[2:3], off offset:2048
	v_add_co_u32_e64 v2, s[0:1], s79, v10
	s_nop 1
	v_addc_co_u32_e64 v3, s[0:1], 0, v11, s[0:1]
	global_load_dwordx4 v[78:81], v[2:3], off offset:2048
	v_add_co_u32_e64 v2, s[0:1], s79, v12
	s_nop 1
	v_addc_co_u32_e64 v3, s[0:1], 0, v13, s[0:1]
	global_load_dwordx4 v[74:77], v[2:3], off offset:2048
	v_add_co_u32_e64 v2, s[0:1], s79, v14
	s_nop 1
	v_addc_co_u32_e64 v3, s[0:1], 0, v15, s[0:1]
	global_load_dwordx4 v[70:73], v[2:3], off offset:2048
	v_add_co_u32_e64 v2, s[0:1], s79, v16
	s_nop 1
	v_addc_co_u32_e64 v3, s[0:1], 0, v17, s[0:1]
	global_load_dwordx4 v[66:69], v[2:3], off offset:2048
	ds_read_u16 v2, v137
	ds_read_u16 v3, v137 offset:512
	s_lshl_b32 s0, s83, 10
	s_mov_b32 s1, s73
	s_cmpk_gt_i32 s82, 0x1ff
	s_waitcnt lgkmcnt(0)
	v_lshl_or_b32 v2, v3, 16, v2
	ds_read_u16 v3, v137 offset:1024
	ds_read_u16 v4, v137 offset:1536
	s_waitcnt lgkmcnt(0)
	v_lshl_or_b32 v3, v4, 16, v3
	ds_read_u16 v4, v137 offset:2048
	ds_read_u16 v5, v137 offset:2560
	s_waitcnt lgkmcnt(0)
	v_lshl_or_b32 v4, v5, 16, v4
	ds_read_u16 v5, v137 offset:3072
	ds_read_u16 v6, v137 offset:3584
	s_waitcnt lgkmcnt(0)
	v_lshl_or_b32 v5, v6, 16, v5
	ds_read_b128 v[6:9], v148
	ds_read_b128 v[150:153], v148 offset:32
	s_waitcnt lgkmcnt(1)
	v_mfma_f32_32x32x16_bf16 v[50:65], v[6:9], v[2:5], 0
	ds_read_b128 v[6:9], v148 offset:8704
	s_waitcnt lgkmcnt(0)
	v_mfma_f32_32x32x16_bf16 v[34:49], v[6:9], v[2:5], 0
	ds_read_b128 v[6:9], v148 offset:17408
	s_waitcnt lgkmcnt(0)
	v_mfma_f32_32x32x16_bf16 v[18:33], v[6:9], v[2:5], 0
	ds_read_b128 v[6:9], v148 offset:26112
	ds_read_u16 v100, v137 offset:8192
	ds_read_u16 v154, v137 offset:8704
	s_waitcnt lgkmcnt(0)
	v_lshl_or_b32 v154, v154, 16, v100
	ds_read_u16 v100, v137 offset:9216
	ds_read_u16 v155, v137 offset:9728
	v_mfma_f32_32x32x16_bf16 v[2:17], v[6:9], v[2:5], 0
	s_waitcnt lgkmcnt(0)
	v_lshl_or_b32 v155, v155, 16, v100
	ds_read_u16 v100, v137 offset:10240
	ds_read_u16 v156, v137 offset:10752
	s_waitcnt lgkmcnt(0)
	v_lshl_or_b32 v156, v156, 16, v100
	ds_read_u16 v100, v137 offset:11264
	ds_read_u16 v157, v137 offset:11776
	s_waitcnt lgkmcnt(0)
	v_lshl_or_b32 v157, v157, 16, v100
	s_nop 1
	v_mfma_f32_32x32x16_bf16 v[50:65], v[150:153], v[154:157], v[50:65]
	ds_read_b128 v[150:153], v148 offset:8736
	s_waitcnt lgkmcnt(0)
	v_mfma_f32_32x32x16_bf16 v[34:49], v[150:153], v[154:157], v[34:49]
	ds_read_b128 v[150:153], v148 offset:17440
	s_waitcnt lgkmcnt(0)
	v_mfma_f32_32x32x16_bf16 v[18:33], v[150:153], v[154:157], v[18:33]
	ds_read_b128 v[150:153], v148 offset:26144
	s_waitcnt lgkmcnt(0)
; #define LAS __attribute__((address_space(3)))
; #define LDS_WAIT() asm volatile("s_waitcnt lgkmcnt(0)" ::: "memory")
; __device__ __forceinline__ void sgu_unit(Frame& F, int unit) {
;     ...
; #pragma unroll
;     for (int ks = 0; ks < 8; ++ks) {
;         v4u xw;
; #pragma unroll
;         for (int j = 0; j < 4; ++j) { const unsigned lo = *(const LAS unsigned short*)(xb + (16 * ks + 2 * j) * 512), hh = *(const LAS unsigned short*)(xb + (16 * ks + 2 * j + 1) * 512); xw[j] = lo | (hh << 16); }
;         const bf16x8 xf = __builtin_bit_cast(bf16x8, xw);
; #pragma unroll
;         for (int tb = 0; tb < 4; ++tb) if (ks < 2 * (tb + 1)) { const bf16x8 wf = *(const LAS bf16x8*)(wa + tb * 32 * SG_STR + ks * 32); acc[tb] = __builtin_amdgcn_mfma_f32_32x32x16_bf16(wf, xf, acc[tb], 0, 0, 0); } }
;     LDS_WAIT(); __builtin_amdgcn_s_barrier(); asm volatile("" ::: "memory");
	v_mfma_f32_32x32x16_bf16 v[2:17], v[150:153], v[154:157], v[2:17]
	ds_read_u16 v100, v137 offset:16384
	ds_read_u16 v150, v137 offset:16896
	s_waitcnt lgkmcnt(0)
	v_lshl_or_b32 v150, v150, 16, v100
	ds_read_u16 v100, v137 offset:17408
	ds_read_u16 v151, v137 offset:17920
	s_waitcnt lgkmcnt(0)
	v_lshl_or_b32 v151, v151, 16, v100
	ds_read_u16 v100, v137 offset:18432
	ds_read_u16 v152, v137 offset:18944
	s_waitcnt lgkmcnt(0)
	v_lshl_or_b32 v152, v152, 16, v100
	ds_read_u16 v100, v137 offset:19456
	ds_read_u16 v153, v137 offset:19968
	ds_read_b128 v[154:157], v148 offset:8768
	s_waitcnt lgkmcnt(1)
	v_lshl_or_b32 v153, v153, 16, v100
	s_waitcnt lgkmcnt(0)
	s_nop 0
	v_mfma_f32_32x32x16_bf16 v[34:49], v[154:157], v[150:153], v[34:49]
	ds_read_b128 v[154:157], v148 offset:17472
	s_waitcnt lgkmcnt(0)
	v_mfma_f32_32x32x16_bf16 v[18:33], v[154:157], v[150:153], v[18:33]
	ds_read_b128 v[154:157], v148 offset:26176
	s_waitcnt lgkmcnt(0)
	v_mfma_f32_32x32x16_bf16 v[2:17], v[154:157], v[150:153], v[2:17]
	ds_read_u16 v100, v137 offset:24576
	ds_read_u16 v150, v137 offset:25088
	s_waitcnt lgkmcnt(0)
	v_lshl_or_b32 v150, v150, 16, v100
	ds_read_u16 v100, v137 offset:25600
	ds_read_u16 v151, v137 offset:26112
	s_waitcnt lgkmcnt(0)
	v_lshl_or_b32 v151, v151, 16, v100
	ds_read_u16 v100, v137 offset:26624
	ds_read_u16 v152, v137 offset:27136
	s_waitcnt lgkmcnt(0)
	v_lshl_or_b32 v152, v152, 16, v100
	ds_read_u16 v100, v137 offset:27648
	ds_read_u16 v153, v137 offset:28160
	ds_read_b128 v[154:157], v148 offset:8800
	s_waitcnt lgkmcnt(1)
	v_lshl_or_b32 v153, v153, 16, v100
	s_waitcnt lgkmcnt(0)
	s_nop 0
	v_mfma_f32_32x32x16_bf16 v[34:49], v[154:157], v[150:153], v[34:49]
	ds_read_b128 v[154:157], v148 offset:17504
	s_waitcnt lgkmcnt(0)
	v_mfma_f32_32x32x16_bf16 v[18:33], v[154:157], v[150:153], v[18:33]
	ds_read_b128 v[154:157], v148 offset:26208
	s_waitcnt lgkmcnt(0)
	v_mfma_f32_32x32x16_bf16 v[2:17], v[154:157], v[150:153], v[2:17]
	ds_read_u16 v100, v137 offset:32768
	ds_read_u16 v150, v137 offset:33280
	s_waitcnt lgkmcnt(0)
	v_lshl_or_b32 v150, v150, 16, v100
	ds_read_u16 v100, v137 offset:33792
	ds_read_u16 v151, v137 offset:34304
	s_waitcnt lgkmcnt(0)
	v_lshl_or_b32 v151, v151, 16, v100
	ds_read_u16 v100, v137 offset:34816
	ds_read_u16 v152, v137 offset:35328
	s_waitcnt lgkmcnt(0)
	v_lshl_or_b32 v152, v152, 16, v100
	ds_read_u16 v100, v137 offset:35840
	ds_read_u16 v153, v137 offset:36352
	ds_read_b128 v[154:157], v148 offset:17536
	s_waitcnt lgkmcnt(1)
	v_lshl_or_b32 v153, v153, 16, v100
	s_waitcnt lgkmcnt(0)
	s_nop 0
	v_mfma_f32_32x32x16_bf16 v[18:33], v[154:157], v[150:153], v[18:33]
	ds_read_b128 v[154:157], v148 offset:26240
	s_waitcnt lgkmcnt(0)
	v_mfma_f32_32x32x16_bf16 v[2:17], v[154:157], v[150:153], v[2:17]
	ds_read_u16 v100, v137 offset:40960
	ds_read_u16 v150, v137 offset:41472
	s_waitcnt lgkmcnt(0)
	v_lshl_or_b32 v150, v150, 16, v100
	ds_read_u16 v100, v137 offset:41984
	ds_read_u16 v151, v137 offset:42496
	s_waitcnt lgkmcnt(0)
	v_lshl_or_b32 v151, v151, 16, v100
	ds_read_u16 v100, v137 offset:43008
	ds_read_u16 v152, v137 offset:43520
	s_waitcnt lgkmcnt(0)
	v_lshl_or_b32 v152, v152, 16, v100
	ds_read_u16 v100, v137 offset:44032
	ds_read_u16 v153, v137 offset:44544
	ds_read_b128 v[154:157], v148 offset:17568
	s_waitcnt lgkmcnt(1)
	v_lshl_or_b32 v153, v153, 16, v100
	s_waitcnt lgkmcnt(0)
	s_nop 0
	v_mfma_f32_32x32x16_bf16 v[18:33], v[154:157], v[150:153], v[18:33]
	ds_read_b128 v[154:157], v148 offset:26272
	s_waitcnt lgkmcnt(0)
	v_mfma_f32_32x32x16_bf16 v[2:17], v[154:157], v[150:153], v[2:17]
	ds_read_u16 v100, v137 offset:49152
	ds_read_u16 v150, v137 offset:49664
	s_waitcnt lgkmcnt(0)
	v_lshl_or_b32 v150, v150, 16, v100
	ds_read_u16 v100, v137 offset:50176
	ds_read_u16 v151, v137 offset:50688
	s_waitcnt lgkmcnt(0)
	v_lshl_or_b32 v151, v151, 16, v100
	ds_read_u16 v100, v137 offset:51200
	ds_read_u16 v152, v137 offset:51712
	s_waitcnt lgkmcnt(0)
	v_lshl_or_b32 v152, v152, 16, v100
	ds_read_u16 v100, v137 offset:52224
	ds_read_u16 v153, v137 offset:52736
	ds_read_b128 v[154:157], v148 offset:26304
	s_waitcnt lgkmcnt(1)
	v_lshl_or_b32 v153, v153, 16, v100
	s_waitcnt lgkmcnt(0)
	s_nop 0
	v_mfma_f32_32x32x16_bf16 v[2:17], v[154:157], v[150:153], v[2:17]
	ds_read_u16 v100, v137 offset:57344
	ds_read_u16 v150, v137 offset:57856
	s_waitcnt lgkmcnt(0)
	v_lshl_or_b32 v150, v150, 16, v100
	ds_read_u16 v100, v137 offset:58368
	ds_read_u16 v151, v137 offset:58880
	s_waitcnt lgkmcnt(0)
	v_lshl_or_b32 v151, v151, 16, v100
	ds_read_u16 v100, v137 offset:59392
	ds_read_u16 v152, v137 offset:59904
	s_waitcnt lgkmcnt(0)
	v_lshl_or_b32 v152, v152, 16, v100
	ds_read_u16 v100, v137 offset:60416
	ds_read_u16 v153, v137 offset:60928
	ds_read_b128 v[154:157], v148 offset:26336
	s_waitcnt lgkmcnt(0)
	s_barrier
; #define GAS __attribute__((address_space(1)))
; #define LAS __attribute__((address_space(3)))
; #define LDS_WAIT() asm volatile("s_waitcnt lgkmcnt(0)" ::: "memory")
; __device__ __forceinline__ unsigned f2bf(float f) { unsigned u = __builtin_bit_cast(unsigned, f); return (u + 0x7fffu + ((u >> 16) & 1u)) >> 16; }
; __device__ __forceinline__ void sgu_unit(Frame& F, int unit) {
;     ...
;     LDS_WAIT(); __builtin_amdgcn_s_barrier(); asm volatile("" ::: "memory");
;     { const int cl = 32 * w + l31;
; #pragma unroll
;       for (int tb = 0; tb < 4; ++tb)
; #pragma unroll
;           for (int r = 0; r < 16; ++r) { const int t = 32 * tb + (r & 3) + 8 * (r >> 2) + 4 * hi; *(LAS unsigned short*)(L + t * 512 + 2 * cl) = (unsigned short)f2bf(acc[tb][r]); } }
;     const f32x4 g0 = *(const GAS f32x4*)(F.sgg + c0 + 8 * q_), g1 = *(const GAS f32x4*)(F.sgg + c0 + 8 * q_ + 4);
;     LDS_WAIT(); __builtin_amdgcn_s_barrier(); asm volatile("" ::: "memory");
	s_waitcnt lgkmcnt(1)
	v_lshl_or_b32 v153, v153, 16, v100
	v_bfe_u32 v100, v50, 16, 1
	v_add3_u32 v50, v50, v100, s80
	ds_write_b16_d16_hi v138, v50
	v_bfe_u32 v50, v51, 16, 1
	v_add3_u32 v50, v51, v50, s80
	ds_write_b16_d16_hi v138, v50 offset:512
	v_bfe_u32 v50, v52, 16, 1
	v_add3_u32 v50, v52, v50, s80
	ds_write_b16_d16_hi v138, v50 offset:1024
	v_bfe_u32 v50, v53, 16, 1
	v_add3_u32 v50, v53, v50, s80
	ds_write_b16_d16_hi v138, v50 offset:1536
	v_bfe_u32 v50, v54, 16, 1
	v_add3_u32 v50, v54, v50, s80
	ds_write_b16_d16_hi v138, v50 offset:4096
	v_bfe_u32 v50, v55, 16, 1
	v_add3_u32 v50, v55, v50, s80
	ds_write_b16_d16_hi v138, v50 offset:4608
	v_bfe_u32 v50, v56, 16, 1
	v_add3_u32 v50, v56, v50, s80
	ds_write_b16_d16_hi v138, v50 offset:5120
	v_bfe_u32 v50, v57, 16, 1
	v_add3_u32 v50, v57, v50, s80
	ds_write_b16_d16_hi v138, v50 offset:5632
	v_bfe_u32 v50, v58, 16, 1
	v_add3_u32 v50, v58, v50, s80
	ds_write_b16_d16_hi v138, v50 offset:8192
	v_bfe_u32 v50, v59, 16, 1
	v_add3_u32 v50, v59, v50, s80
	ds_write_b16_d16_hi v138, v50 offset:8704
	v_bfe_u32 v50, v60, 16, 1
	v_add3_u32 v50, v60, v50, s80
	ds_write_b16_d16_hi v138, v50 offset:9216
	v_bfe_u32 v50, v61, 16, 1
	v_add3_u32 v50, v61, v50, s80
	ds_write_b16_d16_hi v138, v50 offset:9728
	v_bfe_u32 v50, v62, 16, 1
	v_add3_u32 v50, v62, v50, s80
	ds_write_b16_d16_hi v138, v50 offset:12288
	v_bfe_u32 v50, v63, 16, 1
	v_add3_u32 v50, v63, v50, s80
	ds_write_b16_d16_hi v138, v50 offset:12800
	v_bfe_u32 v50, v64, 16, 1
	v_add3_u32 v50, v64, v50, s80
	ds_write_b16_d16_hi v138, v50 offset:13312
	v_bfe_u32 v50, v65, 16, 1
	v_add3_u32 v50, v65, v50, s80
	ds_write_b16_d16_hi v138, v50 offset:13824
	v_bfe_u32 v50, v34, 16, 1
	v_add3_u32 v34, v34, v50, s80
	ds_write_b16_d16_hi v138, v34 offset:16384
	v_bfe_u32 v34, v35, 16, 1
	v_add3_u32 v34, v35, v34, s80
	ds_write_b16_d16_hi v138, v34 offset:16896
	v_bfe_u32 v34, v36, 16, 1
	v_add3_u32 v34, v36, v34, s80
	ds_write_b16_d16_hi v138, v34 offset:17408
	v_bfe_u32 v34, v37, 16, 1
	v_add3_u32 v34, v37, v34, s80
	ds_write_b16_d16_hi v138, v34 offset:17920
	v_bfe_u32 v34, v38, 16, 1
	v_add3_u32 v34, v38, v34, s80
	ds_write_b16_d16_hi v138, v34 offset:20480
	v_bfe_u32 v34, v39, 16, 1
	v_add3_u32 v34, v39, v34, s80
	ds_write_b16_d16_hi v138, v34 offset:20992
	v_bfe_u32 v34, v40, 16, 1
	v_add3_u32 v34, v40, v34, s80
	ds_write_b16_d16_hi v138, v34 offset:21504
	v_bfe_u32 v34, v41, 16, 1
	v_add3_u32 v34, v41, v34, s80
	ds_write_b16_d16_hi v138, v34 offset:22016
	v_bfe_u32 v34, v42, 16, 1
	v_add3_u32 v34, v42, v34, s80
	ds_write_b16_d16_hi v138, v34 offset:24576
	v_bfe_u32 v34, v43, 16, 1
	v_add3_u32 v34, v43, v34, s80
	ds_write_b16_d16_hi v138, v34 offset:25088
	v_bfe_u32 v34, v44, 16, 1
	v_add3_u32 v34, v44, v34, s80
	ds_write_b16_d16_hi v138, v34 offset:25600
	v_bfe_u32 v34, v45, 16, 1
	v_add3_u32 v34, v45, v34, s80
	ds_write_b16_d16_hi v138, v34 offset:26112
	v_bfe_u32 v34, v46, 16, 1
	v_add3_u32 v34, v46, v34, s80
	ds_write_b16_d16_hi v138, v34 offset:28672
	v_bfe_u32 v34, v47, 16, 1
	v_add3_u32 v34, v47, v34, s80
	ds_write_b16_d16_hi v138, v34 offset:29184
	v_bfe_u32 v34, v48, 16, 1
	v_add3_u32 v34, v48, v34, s80
	ds_write_b16_d16_hi v138, v34 offset:29696
	v_bfe_u32 v34, v49, 16, 1
	v_add3_u32 v34, v49, v34, s80
	ds_write_b16_d16_hi v138, v34 offset:30208
	v_bfe_u32 v34, v18, 16, 1
	v_add3_u32 v18, v18, v34, s80
	ds_write_b16_d16_hi v138, v18 offset:32768
	v_bfe_u32 v18, v19, 16, 1
	v_add3_u32 v18, v19, v18, s80
	ds_write_b16_d16_hi v138, v18 offset:33280
	v_bfe_u32 v18, v20, 16, 1
	v_add3_u32 v18, v20, v18, s80
	ds_write_b16_d16_hi v138, v18 offset:33792
	v_bfe_u32 v18, v21, 16, 1
	v_add3_u32 v18, v21, v18, s80
	ds_write_b16_d16_hi v138, v18 offset:34304
	v_bfe_u32 v18, v22, 16, 1
	v_add3_u32 v18, v22, v18, s80
	ds_write_b16_d16_hi v138, v18 offset:36864
	v_bfe_u32 v18, v23, 16, 1
	v_add3_u32 v18, v23, v18, s80
	ds_write_b16_d16_hi v138, v18 offset:37376
	v_bfe_u32 v18, v24, 16, 1
	v_add3_u32 v18, v24, v18, s80
	ds_write_b16_d16_hi v138, v18 offset:37888
	v_bfe_u32 v18, v25, 16, 1
	v_add3_u32 v18, v25, v18, s80
	ds_write_b16_d16_hi v138, v18 offset:38400
	v_bfe_u32 v18, v26, 16, 1
	v_add3_u32 v18, v26, v18, s80
	ds_write_b16_d16_hi v138, v18 offset:40960
	v_bfe_u32 v18, v27, 16, 1
	v_add3_u32 v18, v27, v18, s80
	ds_write_b16_d16_hi v138, v18 offset:41472
	v_bfe_u32 v18, v28, 16, 1
	v_add3_u32 v18, v28, v18, s80
	ds_write_b16_d16_hi v138, v18 offset:41984
	v_bfe_u32 v18, v29, 16, 1
	v_add3_u32 v18, v29, v18, s80
	s_waitcnt lgkmcnt(14)
	v_mfma_f32_32x32x16_bf16 v[2:17], v[154:157], v[150:153], v[2:17]
	ds_write_b16_d16_hi v138, v18 offset:42496
	v_bfe_u32 v18, v30, 16, 1
	v_add3_u32 v18, v30, v18, s80
	ds_write_b16_d16_hi v138, v18 offset:45056
	v_bfe_u32 v18, v31, 16, 1
	v_add3_u32 v18, v31, v18, s80
	ds_write_b16_d16_hi v138, v18 offset:45568
	v_bfe_u32 v18, v32, 16, 1
	v_add3_u32 v18, v32, v18, s80
	ds_write_b16_d16_hi v138, v18 offset:46080
	v_bfe_u32 v18, v33, 16, 1
	v_add3_u32 v18, v33, v18, s80
	ds_write_b16_d16_hi v138, v18 offset:46592
	v_bfe_u32 v18, v2, 16, 1
	v_add3_u32 v2, v2, v18, s80
	ds_write_b16_d16_hi v138, v2 offset:49152
	v_bfe_u32 v2, v3, 16, 1
	v_add3_u32 v2, v3, v2, s80
	ds_write_b16_d16_hi v138, v2 offset:49664
	v_bfe_u32 v2, v4, 16, 1
	v_add3_u32 v2, v4, v2, s80
	ds_write_b16_d16_hi v138, v2 offset:50176
	v_bfe_u32 v2, v5, 16, 1
	v_add3_u32 v2, v5, v2, s80
	ds_write_b16_d16_hi v138, v2 offset:50688
	v_bfe_u32 v2, v6, 16, 1
	v_add3_u32 v2, v6, v2, s80
	ds_write_b16_d16_hi v138, v2 offset:53248
	v_bfe_u32 v2, v7, 16, 1
	v_add3_u32 v2, v7, v2, s80
	ds_write_b16_d16_hi v138, v2 offset:53760
	v_bfe_u32 v2, v8, 16, 1
	v_add3_u32 v2, v8, v2, s80
	ds_write_b16_d16_hi v138, v2 offset:54272
	v_bfe_u32 v2, v9, 16, 1
	v_add3_u32 v2, v9, v2, s80
	ds_write_b16_d16_hi v138, v2 offset:54784
	v_bfe_u32 v2, v10, 16, 1
	v_add3_u32 v2, v10, v2, s80
	ds_write_b16_d16_hi v138, v2 offset:57344
	v_bfe_u32 v2, v11, 16, 1
	v_add3_u32 v2, v11, v2, s80
	ds_write_b16_d16_hi v138, v2 offset:57856
	v_bfe_u32 v2, v12, 16, 1
	v_add3_u32 v2, v12, v2, s80
	ds_write_b16_d16_hi v138, v2 offset:58368
	v_bfe_u32 v2, v13, 16, 1
	v_add3_u32 v2, v13, v2, s80
	ds_write_b16_d16_hi v138, v2 offset:58880
	v_bfe_u32 v2, v14, 16, 1
	v_add3_u32 v2, v14, v2, s80
	ds_write_b16_d16_hi v138, v2 offset:61440
	v_bfe_u32 v2, v15, 16, 1
	v_add3_u32 v2, v15, v2, s80
	ds_write_b16_d16_hi v138, v2 offset:61952
	v_bfe_u32 v2, v16, 16, 1
	v_add3_u32 v2, v16, v2, s80
	ds_write_b16_d16_hi v138, v2 offset:62464
	v_bfe_u32 v2, v17, 16, 1
	v_add3_u32 v2, v17, v2, s80
	ds_write_b16_d16_hi v138, v2 offset:62976
	v_lshl_add_u64 v[6:7], v[106:107], 0, s[0:1]
	global_load_dwordx4 v[2:5], v[6:7], off offset:16
	s_nop 0
	global_load_dwordx4 v[6:9], v[6:7], off
	s_waitcnt lgkmcnt(0)
	s_barrier
; #define GAS __attribute__((address_space(1)))
; #define LAS __attribute__((address_space(3)))
; __device__ __forceinline__ void sgu_unit(Frame& F, int unit) {
;     ...
; #pragma unroll
;     for (int i = 0; i < 8; ++i) { const v4u fw = *(const LAS v4u*)(L + (rs_ + 16 * i) * 512 + q_ * 16); const float bb = F.sgb[g * GMC + rs_ + 16 * i]; v2u o;
;         o.x = pk4_fp8(S_YB * bflo(uu[i].x) * (bflo(fw.x) * g0.x + bb), S_YB * bfhi(uu[i].x) * (bfhi(fw.x) * g0.y + bb), S_YB * bflo(uu[i].y) * (bflo(fw.y) * g0.z + bb), S_YB * bfhi(uu[i].y) * (bfhi(fw.y) * g0.w + bb));
;         o.y = pk4_fp8(S_YB * bflo(uu[i].z) * (bflo(fw.z) * g1.x + bb), S_YB * bfhi(uu[i].z) * (bfhi(fw.z) * g1.y + bb), S_YB * bflo(uu[i].w) * (bflo(fw.w) * g1.z + bb), S_YB * bfhi(uu[i].w) * (bfhi(fw.w) * g1.w + bb));
;         *(GAS v2u*)((unsigned char*)F.YA + (size_t)(r0 + rs_ + 16 * i) * (2 * ATTW) + ATTW + c0 + 8 * q_) = o; }
	v_lshlrev_b32_e32 v20, 2, v113
	global_load_dword v19, v20, s[8:9]
	ds_read_b128 v[10:13], v139
	s_waitcnt vmcnt(10)
	v_lshlrev_b32_e32 v14, 16, v94
	v_lshlrev_b32_e32 v16, 16, v95
	v_lshlrev_b32_e32 v22, 16, v97
	s_waitcnt lgkmcnt(0)
	v_lshlrev_b32_e32 v15, 16, v10
	v_lshlrev_b32_e32 v17, 16, v11
	v_and_b32_e32 v11, 0xffff0000, v11
	v_lshlrev_b32_e32 v23, 16, v13
	v_and_b32_e32 v13, 0xffff0000, v13
	s_waitcnt vmcnt(1)
	v_mov_b32_e32 v113, v6
	v_pk_mul_f32 v[14:15], v[112:113], v[14:15]
	s_waitcnt vmcnt(0)
	v_add_f32_e32 v6, v19, v15
	v_mul_f32_e32 v18, v14, v6
	v_and_b32_e32 v15, 0xffff0000, v10
	v_and_b32_e32 v14, 0xffff0000, v94
	v_mov_b32_e32 v6, v112
	v_pk_mul_f32 v[14:15], v[6:7], v[14:15]
	s_nop 0
	v_add_f32_e32 v10, v19, v15
	v_mul_f32_e32 v21, v14, v10
	v_mov_b32_e32 v14, v112
	v_mov_b32_e32 v15, v8
	v_pk_mul_f32 v[16:17], v[14:15], v[16:17]
	v_and_b32_e32 v10, 0xffff0000, v95
	v_add_f32_e32 v8, v19, v17
	v_mul_f32_e32 v16, v16, v8
	v_mov_b32_e32 v8, v112
	v_pk_mul_f32 v[10:11], v[8:9], v[10:11]
	v_med3_f32 v17, v21, s81, v149
	v_add_f32_e32 v11, v19, v11
	v_mul_f32_e32 v10, v10, v11
	v_med3_f32 v11, v18, s81, v149
	v_mov_b32_e32 v18, v101
	v_cvt_pk_fp8_f32 v18, v11, v17
	v_med3_f32 v11, v16, s81, v149
	v_med3_f32 v10, v10, s81, v149
	v_lshlrev_b32_e32 v16, 16, v96
	v_cvt_pk_fp8_f32 v18, v11, v10 op_sel:[0,0,1]
	v_lshlrev_b32_e32 v17, 16, v12
	v_mov_b32_e32 v10, v112
	v_mov_b32_e32 v11, v2
	v_pk_mul_f32 v[16:17], v[10:11], v[16:17]
	s_nop 0
	v_add_f32_e32 v2, v19, v17
	v_mul_f32_e32 v21, v16, v2
	v_and_b32_e32 v17, 0xffff0000, v12
	v_and_b32_e32 v16, 0xffff0000, v96
	v_mov_b32_e32 v2, v112
	v_pk_mul_f32 v[16:17], v[2:3], v[16:17]
	s_nop 0
	v_add_f32_e32 v12, v19, v17
	v_mul_f32_e32 v24, v16, v12
	v_mov_b32_e32 v16, v112
	v_mov_b32_e32 v17, v4
	v_pk_mul_f32 v[22:23], v[16:17], v[22:23]
	v_and_b32_e32 v12, 0xffff0000, v97
	v_add_f32_e32 v4, v19, v23
	v_mul_f32_e32 v22, v22, v4
	v_mov_b32_e32 v4, v112
	v_pk_mul_f32 v[12:13], v[4:5], v[12:13]
	s_nop 0
	v_add_f32_e32 v13, v19, v13
	v_mul_f32_e32 v12, v12, v13
	v_med3_f32 v13, v21, s81, v149
	v_med3_f32 v21, v24, s81, v149
	v_mov_b32_e32 v19, v101
	v_cvt_pk_fp8_f32 v19, v13, v21
	v_med3_f32 v13, v22, s81, v149
	v_med3_f32 v12, v12, s81, v149
	ds_read_b128 v[22:25], v140
	v_cvt_pk_fp8_f32 v19, v13, v12 op_sel:[0,0,1]
	v_lshlrev_b64 v[12:13], 12, v[128:129]
	v_lshl_add_u64 v[12:13], s[68:69], 0, v[12:13]
	v_lshl_add_u64 v[12:13], v[12:13], 0, s[72:73]
	v_lshl_add_u64 v[12:13], v[12:13], 0, v[98:99]
	global_store_dwordx2 v[12:13], v[18:19], off offset:2048
	global_load_dword v21, v20, s[8:9] offset:64
	v_lshlrev_b32_e32 v12, 16, v90
	s_waitcnt lgkmcnt(0)
	v_lshlrev_b32_e32 v13, 16, v22
	v_pk_mul_f32 v[12:13], v[112:113], v[12:13]
	s_waitcnt vmcnt(0)
	v_add_f32_e32 v13, v21, v13
	v_mul_f32_e32 v18, v12, v13
	v_and_b32_e32 v13, 0xffff0000, v22
	v_and_b32_e32 v12, 0xffff0000, v90
	v_pk_mul_f32 v[12:13], v[6:7], v[12:13]
	v_med3_f32 v18, v18, s81, v149
	v_add_f32_e32 v13, v21, v13
	v_mul_f32_e32 v19, v12, v13
	v_lshlrev_b32_e32 v12, 16, v91
	v_lshlrev_b32_e32 v13, 16, v23
	v_pk_mul_f32 v[12:13], v[14:15], v[12:13]
	v_med3_f32 v19, v19, s81, v149
	v_add_f32_e32 v13, v21, v13
	v_mul_f32_e32 v22, v12, v13
	v_and_b32_e32 v13, 0xffff0000, v23
	v_and_b32_e32 v12, 0xffff0000, v91
	v_pk_mul_f32 v[12:13], v[8:9], v[12:13]
	s_nop 0
	v_add_f32_e32 v13, v21, v13
	v_mul_f32_e32 v13, v12, v13
	v_mov_b32_e32 v12, v101
	v_cvt_pk_fp8_f32 v12, v18, v19
	v_med3_f32 v18, v22, s81, v149
	v_med3_f32 v13, v13, s81, v149
	v_lshlrev_b32_e32 v19, 16, v24
	v_cvt_pk_fp8_f32 v12, v18, v13 op_sel:[0,0,1]
	v_lshlrev_b32_e32 v18, 16, v92
	v_pk_mul_f32 v[18:19], v[10:11], v[18:19]
	s_nop 0
	v_add_f32_e32 v13, v21, v19
	v_mul_f32_e32 v13, v18, v13
	v_and_b32_e32 v19, 0xffff0000, v24
	v_and_b32_e32 v18, 0xffff0000, v92
	v_pk_mul_f32 v[18:19], v[2:3], v[18:19]
	s_nop 0
	v_add_f32_e32 v19, v21, v19
	v_mul_f32_e32 v22, v18, v19
	v_lshlrev_b32_e32 v18, 16, v93
	v_lshlrev_b32_e32 v19, 16, v25
	v_pk_mul_f32 v[18:19], v[16:17], v[18:19]
	s_nop 0
	v_add_f32_e32 v19, v21, v19
	v_mul_f32_e32 v23, v18, v19
	v_and_b32_e32 v19, 0xffff0000, v25
	v_and_b32_e32 v18, 0xffff0000, v93
	v_pk_mul_f32 v[18:19], v[4:5], v[18:19]
	s_nop 0
	v_add_f32_e32 v19, v21, v19
	v_mul_f32_e32 v18, v18, v19
	v_med3_f32 v19, v13, s81, v149
	v_med3_f32 v21, v22, s81, v149
	v_mov_b32_e32 v13, v101
	v_cvt_pk_fp8_f32 v13, v19, v21
	v_med3_f32 v19, v23, s81, v149
	v_med3_f32 v18, v18, s81, v149
	ds_read_b128 v[22:25], v141
	v_cvt_pk_fp8_f32 v13, v19, v18 op_sel:[0,0,1]
	v_lshlrev_b64 v[18:19], 12, v[126:127]
	v_lshl_add_u64 v[18:19], s[68:69], 0, v[18:19]
	v_lshl_add_u64 v[18:19], v[18:19], 0, s[72:73]
	v_lshl_add_u64 v[18:19], v[18:19], 0, v[98:99]
	global_store_dwordx2 v[18:19], v[12:13], off offset:2048
	global_load_dword v21, v20, s[8:9] offset:128
	v_lshlrev_b32_e32 v12, 16, v86
	s_waitcnt lgkmcnt(0)
	v_lshlrev_b32_e32 v13, 16, v22
	v_pk_mul_f32 v[12:13], v[112:113], v[12:13]
	s_waitcnt vmcnt(0)
; #define GAS __attribute__((address_space(1)))
; #define LAS __attribute__((address_space(3)))
; __device__ __forceinline__ void sgu_unit(Frame& F, int unit) {
;     ...
; #pragma unroll
;     for (int i = 0; i < 8; ++i) { const v4u fw = *(const LAS v4u*)(L + (rs_ + 16 * i) * 512 + q_ * 16); const float bb = F.sgb[g * GMC + rs_ + 16 * i]; v2u o;
;         o.x = pk4_fp8(S_YB * bflo(uu[i].x) * (bflo(fw.x) * g0.x + bb), S_YB * bfhi(uu[i].x) * (bfhi(fw.x) * g0.y + bb), S_YB * bflo(uu[i].y) * (bflo(fw.y) * g0.z + bb), S_YB * bfhi(uu[i].y) * (bfhi(fw.y) * g0.w + bb));
;         o.y = pk4_fp8(S_YB * bflo(uu[i].z) * (bflo(fw.z) * g1.x + bb), S_YB * bfhi(uu[i].z) * (bfhi(fw.z) * g1.y + bb), S_YB * bflo(uu[i].w) * (bflo(fw.w) * g1.z + bb), S_YB * bfhi(uu[i].w) * (bfhi(fw.w) * g1.w + bb));
;         *(GAS v2u*)((unsigned char*)F.YA + (size_t)(r0 + rs_ + 16 * i) * (2 * ATTW) + ATTW + c0 + 8 * q_) = o; }
	v_add_f32_e32 v13, v21, v13
	v_mul_f32_e32 v18, v12, v13
	v_and_b32_e32 v13, 0xffff0000, v22
	v_and_b32_e32 v12, 0xffff0000, v86
	v_pk_mul_f32 v[12:13], v[6:7], v[12:13]
	v_med3_f32 v18, v18, s81, v149
	v_add_f32_e32 v13, v21, v13
	v_mul_f32_e32 v19, v12, v13
	v_lshlrev_b32_e32 v12, 16, v87
	v_lshlrev_b32_e32 v13, 16, v23
	v_pk_mul_f32 v[12:13], v[14:15], v[12:13]
	v_med3_f32 v19, v19, s81, v149
	v_add_f32_e32 v13, v21, v13
	v_mul_f32_e32 v22, v12, v13
	v_and_b32_e32 v13, 0xffff0000, v23
	v_and_b32_e32 v12, 0xffff0000, v87
	v_pk_mul_f32 v[12:13], v[8:9], v[12:13]
	s_nop 0
	v_add_f32_e32 v13, v21, v13
	v_mul_f32_e32 v13, v12, v13
	v_mov_b32_e32 v12, v101
	v_cvt_pk_fp8_f32 v12, v18, v19
	v_med3_f32 v18, v22, s81, v149
	v_med3_f32 v13, v13, s81, v149
	v_lshlrev_b32_e32 v19, 16, v24
	v_cvt_pk_fp8_f32 v12, v18, v13 op_sel:[0,0,1]
	v_lshlrev_b32_e32 v18, 16, v88
	v_pk_mul_f32 v[18:19], v[10:11], v[18:19]
	s_nop 0
	v_add_f32_e32 v13, v21, v19
	v_mul_f32_e32 v13, v18, v13
	v_and_b32_e32 v19, 0xffff0000, v24
	v_and_b32_e32 v18, 0xffff0000, v88
	v_pk_mul_f32 v[18:19], v[2:3], v[18:19]
	s_nop 0
	v_add_f32_e32 v19, v21, v19
	v_mul_f32_e32 v22, v18, v19
	v_lshlrev_b32_e32 v18, 16, v89
	v_lshlrev_b32_e32 v19, 16, v25
	v_pk_mul_f32 v[18:19], v[16:17], v[18:19]
	s_nop 0
	v_add_f32_e32 v19, v21, v19
	v_mul_f32_e32 v23, v18, v19
	v_and_b32_e32 v19, 0xffff0000, v25
	v_and_b32_e32 v18, 0xffff0000, v89
	v_pk_mul_f32 v[18:19], v[4:5], v[18:19]
	s_nop 0
	v_add_f32_e32 v19, v21, v19
	v_mul_f32_e32 v18, v18, v19
	v_med3_f32 v19, v13, s81, v149
	v_med3_f32 v21, v22, s81, v149
	v_mov_b32_e32 v13, v101
	v_cvt_pk_fp8_f32 v13, v19, v21
	v_med3_f32 v19, v23, s81, v149
	v_med3_f32 v18, v18, s81, v149
	ds_read_b128 v[22:25], v142
	v_cvt_pk_fp8_f32 v13, v19, v18 op_sel:[0,0,1]
	v_lshlrev_b64 v[18:19], 12, v[124:125]
	v_lshl_add_u64 v[18:19], s[68:69], 0, v[18:19]
	v_lshl_add_u64 v[18:19], v[18:19], 0, s[72:73]
	v_lshl_add_u64 v[18:19], v[18:19], 0, v[98:99]
	global_store_dwordx2 v[18:19], v[12:13], off offset:2048
	global_load_dword v21, v20, s[8:9] offset:192
	v_lshlrev_b32_e32 v12, 16, v82
	s_waitcnt lgkmcnt(0)
	v_lshlrev_b32_e32 v13, 16, v22
	v_pk_mul_f32 v[12:13], v[112:113], v[12:13]
	s_waitcnt vmcnt(0)
	v_add_f32_e32 v13, v21, v13
	v_mul_f32_e32 v18, v12, v13
	v_and_b32_e32 v13, 0xffff0000, v22
	v_and_b32_e32 v12, 0xffff0000, v82
	v_pk_mul_f32 v[12:13], v[6:7], v[12:13]
	v_med3_f32 v18, v18, s81, v149
	v_add_f32_e32 v13, v21, v13
	v_mul_f32_e32 v19, v12, v13
	v_lshlrev_b32_e32 v12, 16, v83
	v_lshlrev_b32_e32 v13, 16, v23
	v_pk_mul_f32 v[12:13], v[14:15], v[12:13]
	v_med3_f32 v19, v19, s81, v149
	v_add_f32_e32 v13, v21, v13
	v_mul_f32_e32 v22, v12, v13
	v_and_b32_e32 v13, 0xffff0000, v23
	v_and_b32_e32 v12, 0xffff0000, v83
	v_pk_mul_f32 v[12:13], v[8:9], v[12:13]
	s_nop 0
	v_add_f32_e32 v13, v21, v13
	v_mul_f32_e32 v13, v12, v13
	v_mov_b32_e32 v12, v101
	v_cvt_pk_fp8_f32 v12, v18, v19
	v_med3_f32 v18, v22, s81, v149
	v_med3_f32 v13, v13, s81, v149
	v_lshlrev_b32_e32 v19, 16, v24
	v_cvt_pk_fp8_f32 v12, v18, v13 op_sel:[0,0,1]
	v_lshlrev_b32_e32 v18, 16, v84
	v_pk_mul_f32 v[18:19], v[10:11], v[18:19]
	s_nop 0
	v_add_f32_e32 v13, v21, v19
	v_mul_f32_e32 v13, v18, v13
	v_and_b32_e32 v19, 0xffff0000, v24
	v_and_b32_e32 v18, 0xffff0000, v84
	v_pk_mul_f32 v[18:19], v[2:3], v[18:19]
	s_nop 0
	v_add_f32_e32 v19, v21, v19
	v_mul_f32_e32 v22, v18, v19
	v_lshlrev_b32_e32 v18, 16, v85
	v_lshlrev_b32_e32 v19, 16, v25
	v_pk_mul_f32 v[18:19], v[16:17], v[18:19]
	s_nop 0
	v_add_f32_e32 v19, v21, v19
	v_mul_f32_e32 v23, v18, v19
	v_and_b32_e32 v19, 0xffff0000, v25
	v_and_b32_e32 v18, 0xffff0000, v85
	v_pk_mul_f32 v[18:19], v[4:5], v[18:19]
	s_nop 0
	v_add_f32_e32 v19, v21, v19
	v_mul_f32_e32 v18, v18, v19
	v_med3_f32 v19, v13, s81, v149
	v_med3_f32 v21, v22, s81, v149
	v_mov_b32_e32 v13, v101
	v_cvt_pk_fp8_f32 v13, v19, v21
	v_med3_f32 v19, v23, s81, v149
	v_med3_f32 v18, v18, s81, v149
	ds_read_b128 v[22:25], v143
	v_cvt_pk_fp8_f32 v13, v19, v18 op_sel:[0,0,1]
	v_lshlrev_b64 v[18:19], 12, v[122:123]
	v_lshl_add_u64 v[18:19], s[68:69], 0, v[18:19]
	v_lshl_add_u64 v[18:19], v[18:19], 0, s[72:73]
	v_lshl_add_u64 v[18:19], v[18:19], 0, v[98:99]
	global_store_dwordx2 v[18:19], v[12:13], off offset:2048
	global_load_dword v21, v20, s[8:9] offset:256
	v_lshlrev_b32_e32 v12, 16, v78
	s_waitcnt lgkmcnt(0)
	v_lshlrev_b32_e32 v13, 16, v22
	v_pk_mul_f32 v[12:13], v[112:113], v[12:13]
	s_waitcnt vmcnt(0)
	v_add_f32_e32 v13, v21, v13
	v_mul_f32_e32 v18, v12, v13
	v_and_b32_e32 v13, 0xffff0000, v22
	v_and_b32_e32 v12, 0xffff0000, v78
	v_pk_mul_f32 v[12:13], v[6:7], v[12:13]
	v_med3_f32 v18, v18, s81, v149
	v_add_f32_e32 v13, v21, v13
	v_mul_f32_e32 v19, v12, v13
	v_lshlrev_b32_e32 v12, 16, v79
	v_lshlrev_b32_e32 v13, 16, v23
	v_pk_mul_f32 v[12:13], v[14:15], v[12:13]
	v_med3_f32 v19, v19, s81, v149
	v_add_f32_e32 v13, v21, v13
	v_mul_f32_e32 v22, v12, v13
	v_and_b32_e32 v13, 0xffff0000, v23
	v_and_b32_e32 v12, 0xffff0000, v79
	v_pk_mul_f32 v[12:13], v[8:9], v[12:13]
	s_nop 0
	v_add_f32_e32 v13, v21, v13
	v_mul_f32_e32 v13, v12, v13
	v_mov_b32_e32 v12, v101
	v_cvt_pk_fp8_f32 v12, v18, v19
	v_med3_f32 v18, v22, s81, v149
	v_med3_f32 v13, v13, s81, v149
	v_lshlrev_b32_e32 v19, 16, v24
	v_cvt_pk_fp8_f32 v12, v18, v13 op_sel:[0,0,1]
	v_lshlrev_b32_e32 v18, 16, v80
	v_pk_mul_f32 v[18:19], v[10:11], v[18:19]
	s_nop 0
	v_add_f32_e32 v13, v21, v19
	v_mul_f32_e32 v13, v18, v13
	v_and_b32_e32 v19, 0xffff0000, v24
	v_and_b32_e32 v18, 0xffff0000, v80
	v_pk_mul_f32 v[18:19], v[2:3], v[18:19]
	s_nop 0
	v_add_f32_e32 v19, v21, v19
	v_mul_f32_e32 v22, v18, v19
	v_lshlrev_b32_e32 v18, 16, v81
	v_lshlrev_b32_e32 v19, 16, v25
	v_pk_mul_f32 v[18:19], v[16:17], v[18:19]
	s_nop 0
	v_add_f32_e32 v19, v21, v19
	v_mul_f32_e32 v23, v18, v19
	v_and_b32_e32 v19, 0xffff0000, v25
	v_and_b32_e32 v18, 0xffff0000, v81
	v_pk_mul_f32 v[18:19], v[4:5], v[18:19]
	s_nop 0
	v_add_f32_e32 v19, v21, v19
	v_mul_f32_e32 v18, v18, v19
	v_med3_f32 v19, v13, s81, v149
	v_med3_f32 v21, v22, s81, v149
	v_mov_b32_e32 v13, v101
	v_cvt_pk_fp8_f32 v13, v19, v21
	v_med3_f32 v19, v23, s81, v149
	v_med3_f32 v18, v18, s81, v149
	ds_read_b128 v[22:25], v144
	v_cvt_pk_fp8_f32 v13, v19, v18 op_sel:[0,0,1]
	v_lshlrev_b64 v[18:19], 12, v[120:121]
	v_lshl_add_u64 v[18:19], s[68:69], 0, v[18:19]
	v_lshl_add_u64 v[18:19], v[18:19], 0, s[72:73]
	v_lshl_add_u64 v[18:19], v[18:19], 0, v[98:99]
	global_store_dwordx2 v[18:19], v[12:13], off offset:2048
	global_load_dword v21, v20, s[8:9] offset:320
	v_lshlrev_b32_e32 v12, 16, v74
	s_waitcnt lgkmcnt(0)
; #define GAS __attribute__((address_space(1)))
; #define LAS __attribute__((address_space(3)))
; __device__ __forceinline__ void sgu_unit(Frame& F, int unit) {
;     ...
; #pragma unroll
;     for (int i = 0; i < 8; ++i) { const v4u fw = *(const LAS v4u*)(L + (rs_ + 16 * i) * 512 + q_ * 16); const float bb = F.sgb[g * GMC + rs_ + 16 * i]; v2u o;
;         o.x = pk4_fp8(S_YB * bflo(uu[i].x) * (bflo(fw.x) * g0.x + bb), S_YB * bfhi(uu[i].x) * (bfhi(fw.x) * g0.y + bb), S_YB * bflo(uu[i].y) * (bflo(fw.y) * g0.z + bb), S_YB * bfhi(uu[i].y) * (bfhi(fw.y) * g0.w + bb));
;         o.y = pk4_fp8(S_YB * bflo(uu[i].z) * (bflo(fw.z) * g1.x + bb), S_YB * bfhi(uu[i].z) * (bfhi(fw.z) * g1.y + bb), S_YB * bflo(uu[i].w) * (bflo(fw.w) * g1.z + bb), S_YB * bfhi(uu[i].w) * (bfhi(fw.w) * g1.w + bb));
;         *(GAS v2u*)((unsigned char*)F.YA + (size_t)(r0 + rs_ + 16 * i) * (2 * ATTW) + ATTW + c0 + 8 * q_) = o; }
; }
; __global__ void __launch_bounds__(NWAVES * 64, 2) mega_fwd(Args args) {
;     ...
;         for (int u = blockIdx.x; u < 512; u += F.G) sgu_unit(F, u);
	v_lshlrev_b32_e32 v13, 16, v22
	v_pk_mul_f32 v[12:13], v[112:113], v[12:13]
	s_waitcnt vmcnt(0)
	v_add_f32_e32 v13, v21, v13
	v_mul_f32_e32 v18, v12, v13
	v_and_b32_e32 v13, 0xffff0000, v22
	v_and_b32_e32 v12, 0xffff0000, v74
	v_pk_mul_f32 v[12:13], v[6:7], v[12:13]
	v_med3_f32 v18, v18, s81, v149
	v_add_f32_e32 v13, v21, v13
	v_mul_f32_e32 v19, v12, v13
	v_lshlrev_b32_e32 v12, 16, v75
	v_lshlrev_b32_e32 v13, 16, v23
	v_pk_mul_f32 v[12:13], v[14:15], v[12:13]
	v_med3_f32 v19, v19, s81, v149
	v_add_f32_e32 v13, v21, v13
	v_mul_f32_e32 v22, v12, v13
	v_and_b32_e32 v13, 0xffff0000, v23
	v_and_b32_e32 v12, 0xffff0000, v75
	v_pk_mul_f32 v[12:13], v[8:9], v[12:13]
	s_nop 0
	v_add_f32_e32 v13, v21, v13
	v_mul_f32_e32 v13, v12, v13
	v_mov_b32_e32 v12, v101
	v_cvt_pk_fp8_f32 v12, v18, v19
	v_med3_f32 v18, v22, s81, v149
	v_med3_f32 v13, v13, s81, v149
	v_lshlrev_b32_e32 v19, 16, v24
	v_cvt_pk_fp8_f32 v12, v18, v13 op_sel:[0,0,1]
	v_lshlrev_b32_e32 v18, 16, v76
	v_pk_mul_f32 v[18:19], v[10:11], v[18:19]
	s_nop 0
	v_add_f32_e32 v13, v21, v19
	v_mul_f32_e32 v13, v18, v13
	v_and_b32_e32 v19, 0xffff0000, v24
	v_and_b32_e32 v18, 0xffff0000, v76
	v_pk_mul_f32 v[18:19], v[2:3], v[18:19]
	s_nop 0
	v_add_f32_e32 v19, v21, v19
	v_mul_f32_e32 v22, v18, v19
	v_lshlrev_b32_e32 v18, 16, v77
	v_lshlrev_b32_e32 v19, 16, v25
	v_pk_mul_f32 v[18:19], v[16:17], v[18:19]
	s_nop 0
	v_add_f32_e32 v19, v21, v19
	v_mul_f32_e32 v23, v18, v19
	v_and_b32_e32 v19, 0xffff0000, v25
	v_and_b32_e32 v18, 0xffff0000, v77
	v_pk_mul_f32 v[18:19], v[4:5], v[18:19]
	s_nop 0
	v_add_f32_e32 v19, v21, v19
	v_mul_f32_e32 v18, v18, v19
	v_med3_f32 v19, v13, s81, v149
	v_med3_f32 v21, v22, s81, v149
	v_mov_b32_e32 v13, v101
	v_cvt_pk_fp8_f32 v13, v19, v21
	v_med3_f32 v19, v23, s81, v149
	v_med3_f32 v18, v18, s81, v149
	ds_read_b128 v[22:25], v145
	v_cvt_pk_fp8_f32 v13, v19, v18 op_sel:[0,0,1]
	v_lshlrev_b64 v[18:19], 12, v[118:119]
	v_lshl_add_u64 v[18:19], s[68:69], 0, v[18:19]
	v_lshl_add_u64 v[18:19], v[18:19], 0, s[72:73]
	v_lshl_add_u64 v[18:19], v[18:19], 0, v[98:99]
	global_store_dwordx2 v[18:19], v[12:13], off offset:2048
	global_load_dword v21, v20, s[8:9] offset:384
	v_lshlrev_b32_e32 v12, 16, v70
	s_waitcnt lgkmcnt(0)
	v_lshlrev_b32_e32 v13, 16, v22
	v_pk_mul_f32 v[12:13], v[112:113], v[12:13]
	s_waitcnt vmcnt(0)
	v_add_f32_e32 v13, v21, v13
	v_mul_f32_e32 v18, v12, v13
	v_and_b32_e32 v13, 0xffff0000, v22
	v_and_b32_e32 v12, 0xffff0000, v70
	v_pk_mul_f32 v[12:13], v[6:7], v[12:13]
	v_med3_f32 v18, v18, s81, v149
	v_add_f32_e32 v13, v21, v13
	v_mul_f32_e32 v19, v12, v13
	v_lshlrev_b32_e32 v12, 16, v71
	v_lshlrev_b32_e32 v13, 16, v23
	v_pk_mul_f32 v[12:13], v[14:15], v[12:13]
	v_med3_f32 v19, v19, s81, v149
	v_add_f32_e32 v13, v21, v13
	v_mul_f32_e32 v22, v12, v13
	v_and_b32_e32 v13, 0xffff0000, v23
	v_and_b32_e32 v12, 0xffff0000, v71
	v_pk_mul_f32 v[12:13], v[8:9], v[12:13]
	s_nop 0
	v_add_f32_e32 v13, v21, v13
	v_mul_f32_e32 v13, v12, v13
	v_mov_b32_e32 v12, v101
	v_cvt_pk_fp8_f32 v12, v18, v19
	v_med3_f32 v18, v22, s81, v149
	v_med3_f32 v13, v13, s81, v149
	v_lshlrev_b32_e32 v19, 16, v24
	v_cvt_pk_fp8_f32 v12, v18, v13 op_sel:[0,0,1]
	v_lshlrev_b32_e32 v18, 16, v72
	v_pk_mul_f32 v[18:19], v[10:11], v[18:19]
	s_nop 0
	v_add_f32_e32 v13, v21, v19
	v_mul_f32_e32 v13, v18, v13
	v_and_b32_e32 v19, 0xffff0000, v24
	v_and_b32_e32 v18, 0xffff0000, v72
	v_pk_mul_f32 v[18:19], v[2:3], v[18:19]
	s_nop 0
	v_add_f32_e32 v19, v21, v19
	v_mul_f32_e32 v22, v18, v19
	v_lshlrev_b32_e32 v18, 16, v73
	v_lshlrev_b32_e32 v19, 16, v25
	v_pk_mul_f32 v[18:19], v[16:17], v[18:19]
	s_nop 0
	v_add_f32_e32 v19, v21, v19
	v_mul_f32_e32 v23, v18, v19
	v_and_b32_e32 v19, 0xffff0000, v25
	v_and_b32_e32 v18, 0xffff0000, v73
	v_pk_mul_f32 v[18:19], v[4:5], v[18:19]
	s_nop 0
	v_add_f32_e32 v19, v21, v19
	v_mul_f32_e32 v18, v18, v19
	v_med3_f32 v19, v13, s81, v149
	v_med3_f32 v21, v22, s81, v149
	v_mov_b32_e32 v13, v101
	v_cvt_pk_fp8_f32 v13, v19, v21
	v_med3_f32 v19, v23, s81, v149
	v_med3_f32 v18, v18, s81, v149
	ds_read_b128 v[22:25], v146
	v_cvt_pk_fp8_f32 v13, v19, v18 op_sel:[0,0,1]
	v_lshlrev_b64 v[18:19], 12, v[116:117]
	v_lshl_add_u64 v[18:19], s[68:69], 0, v[18:19]
	v_lshl_add_u64 v[18:19], v[18:19], 0, s[72:73]
	v_lshl_add_u64 v[18:19], v[18:19], 0, v[98:99]
	global_store_dwordx2 v[18:19], v[12:13], off offset:2048
	global_load_dword v18, v20, s[8:9] offset:448
	v_lshlrev_b32_e32 v12, 16, v66
	s_waitcnt lgkmcnt(0)
	v_lshlrev_b32_e32 v13, 16, v22
	v_pk_mul_f32 v[12:13], v[112:113], v[12:13]
	s_waitcnt vmcnt(0)
	v_add_f32_e32 v13, v18, v13
	v_mul_f32_e32 v19, v12, v13
	v_and_b32_e32 v13, 0xffff0000, v22
	v_and_b32_e32 v12, 0xffff0000, v66
	v_pk_mul_f32 v[6:7], v[6:7], v[12:13]
	s_nop 0
	v_add_f32_e32 v7, v18, v7
	v_mul_f32_e32 v12, v6, v7
	v_lshlrev_b32_e32 v6, 16, v67
	v_lshlrev_b32_e32 v7, 16, v23
	v_pk_mul_f32 v[6:7], v[14:15], v[6:7]
	s_nop 0
	v_add_f32_e32 v7, v18, v7
	v_mul_f32_e32 v13, v6, v7
	v_and_b32_e32 v7, 0xffff0000, v23
	v_and_b32_e32 v6, 0xffff0000, v67
	v_pk_mul_f32 v[6:7], v[8:9], v[6:7]
	v_med3_f32 v8, v19, s81, v149
	v_add_f32_e32 v7, v18, v7
	v_mul_f32_e32 v7, v6, v7
	v_med3_f32 v9, v12, s81, v149
	v_mov_b32_e32 v6, v101
	v_cvt_pk_fp8_f32 v6, v8, v9
	v_med3_f32 v8, v13, s81, v149
	v_med3_f32 v7, v7, s81, v149
	v_lshlrev_b32_e32 v9, 16, v24
	v_cvt_pk_fp8_f32 v6, v8, v7 op_sel:[0,0,1]
	v_lshlrev_b32_e32 v8, 16, v68
	v_pk_mul_f32 v[8:9], v[10:11], v[8:9]
	s_nop 0
	v_add_f32_e32 v7, v18, v9
	v_mul_f32_e32 v7, v8, v7
	v_and_b32_e32 v9, 0xffff0000, v24
	v_and_b32_e32 v8, 0xffff0000, v68
	v_pk_mul_f32 v[2:3], v[2:3], v[8:9]
	s_nop 0
	v_add_f32_e32 v3, v18, v3
	v_mul_f32_e32 v8, v2, v3
	v_lshlrev_b32_e32 v2, 16, v69
	v_lshlrev_b32_e32 v3, 16, v25
	v_pk_mul_f32 v[2:3], v[16:17], v[2:3]
	s_nop 0
	v_add_f32_e32 v3, v18, v3
	v_mul_f32_e32 v9, v2, v3
	v_and_b32_e32 v3, 0xffff0000, v25
	v_and_b32_e32 v2, 0xffff0000, v69
	v_pk_mul_f32 v[2:3], v[4:5], v[2:3]
	v_med3_f32 v4, v8, s81, v149
	v_add_f32_e32 v3, v18, v3
	v_mul_f32_e32 v2, v2, v3
	v_med3_f32 v3, v7, s81, v149
	v_mov_b32_e32 v7, v101
	v_cvt_pk_fp8_f32 v7, v3, v4
	v_med3_f32 v3, v9, s81, v149
	v_med3_f32 v2, v2, s81, v149
	v_cvt_pk_fp8_f32 v7, v3, v2 op_sel:[0,0,1]
	v_lshlrev_b64 v[2:3], 12, v[114:115]
	v_lshl_add_u64 v[2:3], s[68:69], 0, v[2:3]
	v_lshl_add_u64 v[2:3], v[2:3], 0, s[72:73]
	v_lshl_add_u64 v[2:3], v[2:3], 0, v[98:99]
	global_store_dwordx2 v[2:3], v[6:7], off offset:2048
	s_cbranch_scc0 .LBB0_1330
